# baseline (speedup 1.0000x reference)
_Z11main_kernelPKfPKiPK15HIP_vector_typeIjLj4EES0_PfS7_S2_i:
	v_and_b32_e32 v104, 0x3ff, v0
	s_mul_i32 s2, s2, 12
	v_readfirstlane_b32 s3, v104
	s_lshr_b32 s3, s3, 6
	s_add_i32 s2, s3, s2
	s_load_dwordx8 s[12:19], s[0:1], 0x0
	s_load_dwordx2 s[10:11], s[0:1], 0x30
	s_mul_i32 s2, s2, 0xf424
	s_mul_hi_u32 s4, s2, 0xaaaaaaab
	s_add_i32 s2, s2, 0xf424
	s_mul_hi_u32 s2, s2, 0xaaaaaaab
	s_lshr_b32 s42, s2, 11
	s_lshl_b32 s2, s3, 8
	v_and_b32_e32 v1, 15, v0
	v_bfe_u32 v112, v0, 4, 2
	s_lshr_b32 s44, s4, 11
	s_lshl_b32 s33, s3, 13
	s_add_i32 s43, s2, 0x20000
	s_sub_u32 s60, s42, s44
	s_cmp_lt_u32 s60, 21
	s_cbranch_scc1 .Lmain_noprio
	s_nop 0
